# grid barrier: XCD leader no longer waits for the ack of its generation bump (on top of mixer rewrite + flat release)
# baseline (speedup 1.0000x reference)
.LBB0_111:
	s_or_b64 exec, exec, s[0:1]
	s_mov_b64 s[0:1], exec
	v_mbcnt_lo_u32_b32 v2, s0, 0
	v_mbcnt_hi_u32_b32 v2, s1, v2
	v_cmp_eq_u32_e32 vcc, 0, v2
	s_and_saveexec_b64 s[4:5], vcc
	s_cbranch_execz .LBB0_113
	s_bcnt1_i32_b64 s0, s[0:1]
	v_mov_b32_e32 v2, s0
.LBB0_113:
	s_or_b64 exec, exec, s[4:5]
.LBB0_114:
	s_or_b64 exec, exec, s[2:3]
	s_waitcnt lgkmcnt(0)
	v_mov_b32_e32 v2, v0
	s_mov_b64 s[0:1], s[42:43]
	s_mov_b32 s4, s95
	s_mov_b32 s3, s85
	s_barrier
	s_lshl_b32 s4, s4, 3
	v_readfirstlane_b32 s2, v2
	s_ashr_i32 s2, s2, 6
	s_add_i32 s5, s4, s2
	s_cmp_gt_i32 s5, 0x83ff
	s_cbranch_scc1 .LBB0_121
	v_lshlrev_b32_e32 v2, 4, v2
	s_add_u32 s12, s0, 0x10000
	v_and_b32_e32 v68, 0x3f0, v2
	s_addc_u32 s13, s1, 0
	v_lshl_add_u64 v[2:3], s[0:1], 0, v[68:69]
	s_mov_b64 s[0:1], 0x18acc000
	v_lshl_add_u64 v[2:3], v[2:3], 0, s[0:1]
	s_lshl_b32 s14, s3, 3
	s_ashr_i32 s1, s2, 31
	s_ashr_i32 s3, s4, 31
	s_add_u32 s0, s2, s4
	s_addc_u32 s1, s1, s3
	s_ashr_i32 s15, s14, 31
	v_lshlrev_b32_e32 v68, 2, v68
	s_branch .LBB0_117

.LBB0_172:
	s_or_b64 exec, exec, s[4:5]
.LBB0_173:
	s_or_b64 exec, exec, s[2:3]
	s_mov_b64 s[8:9], 0x4c000
	s_mov_b64 s[6:7], 0x18acc000
	s_cmp_eq_u32 s36, 0
	s_cbranch_scc1 .Lseam1_l0
	s_mov_b64 s[6:7], 0x14a8c000
	s_mov_b64 s[8:9], 0x89cc000

.LBB0_482:
	s_or_b64 exec, exec, s[4:5]
.LBB0_483:
	s_or_b64 exec, exec, s[2:3]
	v_mov_b32_e32 v20, v0
	s_mov_b64 s[18:19], s[42:43]
	s_mov_b32 s28, s85
	s_mov_b32 s29, s95
	s_waitcnt lgkmcnt(0)
	v_mov_b32_e32 v2, 0x23f30
	s_barrier
	s_lshl_b32 s4, s36, 1
	v_add_u32_e32 v2, 0, v2
	ds_read_b64 v[2:3], v2
	v_ashrrev_i32_e32 v6, 8, v20
	v_lshlrev_b32_e32 v22, 4, v20
	v_and_b32_e32 v7, 0xf00, v22
	s_and_b32 s30, s29, 3
	s_waitcnt lgkmcnt(0)
	v_readfirstlane_b32 s0, v2
	v_add_u32_e32 v2, s4, v6
	v_readfirstlane_b32 s1, v3
	v_ashrrev_i32_e32 v3, 31, v2
	v_lshlrev_b64 v[2:3], 14, v[2:3]
	v_lshl_add_u64 v[2:3], s[0:1], 0, v[2:3]
	v_lshlrev_b32_e32 v68, 2, v7
	v_lshl_add_u64 v[2:3], v[2:3], 0, v[68:69]
	s_lshl_b32 s0, s30, 8
	s_mov_b32 s1, s67
	v_lshl_add_u64 v[2:3], v[2:3], 0, s[0:1]
	v_and_b32_e32 v68, 0xf0, v22
	v_lshl_add_u64 v[2:3], v[2:3], 0, v[68:69]
	global_load_dwordx4 v[2:5], v[2:3], off
	v_lshl_add_u32 v6, v6, 12, 0
	s_movk_i32 s1, 0x80
	v_and_b32_e32 v21, 63, v20
	v_readfirstlane_b32 s6, v20
	s_lshl_b32 s7, s30, 6
	v_add3_u32 v6, v6, v7, v68
	v_cmp_gt_i32_e32 vcc, s1, v20
	s_waitcnt vmcnt(0)
	ds_write_b128 v6, v[2:5] offset:8704
	s_and_saveexec_b64 s[2:3], vcc
	s_cbranch_execz .LBB0_485
	v_mov_b32_e32 v2, 0x23f38
	v_lshrrev_b32_e32 v4, 6, v20
	v_add_u32_e32 v2, 0, v2
	ds_read_b64 v[2:3], v2
	v_add_lshl_u32 v4, v4, s4, 8
	v_or3_b32 v4, v4, v21, s7
	v_ashrrev_i32_e32 v5, 31, v4
	s_waitcnt lgkmcnt(0)
	v_readfirstlane_b32 s1, v3
	v_readfirstlane_b32 s4, v2
	s_nop 0
	v_mov_b32_e32 v3, s1
	v_mov_b32_e32 v2, s4
	v_lshl_add_u64 v[2:3], v[4:5], 2, v[2:3]
	global_load_dword v2, v[2:3], off
	v_lshl_add_u32 v3, v20, 2, 0
	s_waitcnt vmcnt(0)
	ds_write_b32 v3, v2 offset:16896

.LBB0_585:
	s_or_b64 exec, exec, s[4:5]
.LBB0_586:
	s_or_b64 exec, exec, s[2:3]
	s_waitcnt lgkmcnt(0)
	v_mov_b32_e32 v2, v0
	s_mov_b64 s[2:3], s[42:43]
	s_mov_b32 s1, s95
	s_mov_b32 s6, s85
	s_barrier
	s_mov_b32 s0, 0x20000
	v_lshl_add_u32 v34, s1, 9, v2
	v_cmp_gt_i32_e32 vcc, s0, v34
	s_and_saveexec_b64 s[4:5], vcc
	s_cbranch_execz .LBB0_591
	v_lshlrev_b32_e32 v2, 1, v2
	s_lshl_b32 s0, s6, 9
	v_lshl_add_u32 v35, s1, 10, v2
	s_lshl_b32 s1, s6, 10
	s_mov_b64 s[6:7], 0

.LBB0_642:
	s_or_b64 exec, exec, s[4:5]
.LBB0_643:
	s_or_b64 exec, exec, s[2:3]
	v_readlane_b32 s0, v247, 32
	v_readlane_b32 s1, v247, 33
	s_and_b64 s[0:1], s[0:1], exec
	v_mov_b32_e32 v35, v0
	s_mov_b64 s[38:39], s[42:43]
	s_mov_b32 s0, s95
	s_mov_b32 s1, s85
	s_waitcnt lgkmcnt(0)
	v_mov_b32_e32 v2, 0x23f40
	s_barrier
	s_cselect_b32 s44, 0, 4
	v_add_u32_e32 v2, 0, v2
	ds_read_b64 v[2:3], v2
	s_xor_b32 s45, s44, 0x84
	v_readfirstlane_b32 s10, v35
	s_lshl_b32 s48, s45, 2
	s_ashr_i32 s4, s10, 6
	s_add_u32 s40, s38, 0x411f2100
	s_addc_u32 s41, s39, 0
	s_waitcnt lgkmcnt(0)
	v_readfirstlane_b32 s12, v2
	v_cvt_f32_ubyte0_e32 v2, s45
	s_add_u32 s6, s38, 0x52a72100
	v_rcp_iflag_f32_e32 v34, v2
	s_addc_u32 s7, s39, 0
	s_and_b32 s49, s0, 3
	s_waitcnt lgkmcnt(0)
	s_barrier
	s_ashr_i32 s84, s0, 2
	s_cmp_lt_i32 s84, s48
	v_and_b32_e32 v67, 63, v35
	v_readfirstlane_b32 s11, v3
	s_cselect_b64 s[8:9], -1, 0
	s_cmp_ge_i32 s84, s48
	s_cbranch_scc1 .LBB0_658
	v_mul_f32_e32 v2, 0x4f7ffffe, v34
	v_cvt_u32_f32_e32 v2, v2
	s_sub_i32 s2, 0, s45
	s_abs_i32 s1, s84
	s_ashr_i32 s0, s84, 31
	v_readfirstlane_b32 s3, v2
	s_mul_i32 s2, s2, s3
	s_mul_hi_u32 s2, s3, s2
	s_add_i32 s3, s3, s2
	s_mul_hi_u32 s2, s1, s3
	s_mul_i32 s3, s2, s45
	s_sub_i32 s1, s1, s3
	s_add_i32 s3, s2, 1
	s_sub_i32 s5, s1, s45
	s_cmp_ge_u32 s1, s45
	s_cselect_b32 s2, s3, s2
	s_cselect_b32 s1, s5, s1
	s_add_i32 s3, s2, 1
	s_cmp_ge_u32 s1, s45
	s_cselect_b32 s1, s3, s2
	s_xor_b32 s1, s1, s0
	s_sub_i32 s13, s1, s0
	s_mul_i32 s0, s13, s45
	s_sub_i32 s5, s84, s0
	s_add_i32 s5, s5, s44
	s_cmp_lt_i32 s5, 4
	s_cselect_b64 s[0:1], -1, 0
	s_cmp_gt_i32 s5, 3
	s_mov_b64 s[2:3], -1
	s_cbranch_scc1 .LBB0_646
	s_lshl_b32 s2, s13, 8
	s_lshl_b32 s3, s5, 6
	s_add_i32 s14, s3, s2
	s_mov_b64 s[2:3], 0

.LBB0_760:
	s_or_b64 exec, exec, s[4:5]
.LBB0_761:
	s_or_b64 exec, exec, s[2:3]
	v_mov_b32_e32 v4, v0
	s_waitcnt lgkmcnt(0)
	s_barrier
	s_lshr_b32 s96, s23, 8
	s_lshr_b32 s66, s23, 6
	s_mov_b64 s[0:1], s[42:43]
	s_mov_b32 s7, s95
	s_mov_b32 s6, s85
	v_cmp_gt_i32_e32 vcc, 24, v4
	s_barrier
	s_and_saveexec_b64 s[0:1], vcc
	s_cbranch_execz .LBB0_765
	s_ashr_i32 s2, s7, 31
	v_mov_b32_e32 v2, s7
	v_mov_b32_e32 v3, s2
	v_mad_i64_i32 v[2:3], s[2:3], s6, v4, v[2:3]
	v_cmp_gt_i64_e32 vcc, s[66:67], v[2:3]
	s_and_saveexec_b64 s[4:5], vcc
	s_cbranch_execz .LBB0_764
	v_ashrrev_i32_e32 v3, 31, v2
	v_lshrrev_b32_e32 v3, 29, v3
	v_add_u32_e32 v3, v2, v3
	v_ashrrev_i32_e32 v5, 3, v3
	v_and_b32_e32 v3, -8, v3
	v_sub_u32_e32 v2, v2, v3
	s_lshr_b32 s2, s23, 9
	v_lshrrev_b32_e32 v3, 31, v2
	v_or_b32_e32 v3, s2, v3
	v_mul_lo_u32 v2, v3, v2
	v_add_u32_e32 v2, v2, v5
	v_ashrrev_i32_e32 v3, 31, v2
	v_lshrrev_b32_e32 v3, 27, v3
	v_add_u32_e32 v3, v2, v3
	v_ashrrev_i32_e32 v5, 5, v3
	v_lshlrev_b32_e32 v5, 3, v5
	s_waitcnt vmcnt(6)
	v_sub_u32_e32 v6, s96, v5
	v_min_i32_e32 v6, 8, v6
	v_sub_u32_e32 v7, 0, v6
	v_max_i32_e32 v7, v6, v7
	v_cvt_f32_u32_e32 v8, v7
	v_and_b32_e32 v3, 0xffffffe0, v3
	s_waitcnt vmcnt(5)
	v_sub_u32_e32 v10, 0, v7
	v_sub_u32_e32 v2, v2, v3
	v_rcp_iflag_f32_e32 v8, v8
	v_sub_u32_e32 v3, 0, v2
	v_max_i32_e32 v3, v2, v3
	v_xor_b32_e32 v9, v2, v6
	v_mul_f32_e32 v8, 0x4f7ffffe, v8
	v_cvt_u32_f32_e32 v8, v8
	v_ashrrev_i32_e32 v9, 31, v9
	v_mul_lo_u32 v10, v10, v8
	v_mul_hi_u32 v10, v8, v10
	v_add_u32_e32 v8, v8, v10
	v_mul_hi_u32 v8, v3, v8
	v_mul_lo_u32 v10, v8, v7
	v_sub_u32_e32 v3, v3, v10
	v_add_u32_e32 v10, 1, v8
	v_cmp_ge_u32_e64 s[2:3], v3, v7
	s_nop 1
	v_cndmask_b32_e64 v8, v8, v10, s[2:3]
	v_sub_u32_e32 v10, v3, v7
	v_cndmask_b32_e64 v3, v3, v10, s[2:3]
	v_add_u32_e32 v10, 1, v8
	v_cmp_ge_u32_e64 s[2:3], v3, v7
	s_nop 1
	v_cndmask_b32_e64 v3, v8, v10, s[2:3]
	v_xor_b32_e32 v3, v3, v9
	v_sub_u32_e32 v3, v3, v9
	v_mul_lo_u32 v6, v3, v6
	v_sub_u32_e32 v2, v2, v6
	v_add_u32_e32 v5, v2, v5

.LBB0_873:
	s_or_b64 exec, exec, s[4:5]
.LBB0_874:
	s_or_b64 exec, exec, s[2:3]
	v_mov_b32_e32 v34, v0
	s_mov_b64 s[6:7], s[42:43]
	s_mov_b32 s11, s95
	s_mov_b32 s10, s85
	s_waitcnt lgkmcnt(0)
	v_mov_b32_e32 v2, 0x23f50
	s_barrier
	s_mov_b32 s25, s67
	v_add_u32_e32 v2, 0, v2
	ds_read_b64 v[2:3], v2
	s_lshl_b64 s[0:1], s[24:25], 12
	v_and_b32_e32 v38, 63, v34
	v_lshlrev_b32_e32 v30, 6, v38
	v_mov_b32_e32 v18, 0x23f58
	s_waitcnt lgkmcnt(0)
	v_readfirstlane_b32 s2, v2
	v_readfirstlane_b32 s3, v3
	s_add_u32 s2, s2, s0
	s_addc_u32 s3, s3, s1
	s_nop 2
	global_load_dwordx4 v[2:5], v30, s[2:3] offset:48
	global_load_dwordx4 v[6:9], v30, s[2:3] offset:32
	global_load_dwordx4 v[10:13], v30, s[2:3] offset:16
	global_load_dwordx4 v[14:17], v30, s[2:3]
	s_mul_i32 s77, s24, 0x1e000
	v_add_u32_e32 v18, 0, v18
	ds_read_b64 v[18:19], v18
	v_readfirstlane_b32 s12, v34
	s_waitcnt lgkmcnt(0)
	v_readfirstlane_b32 s3, v18
	v_readfirstlane_b32 s2, v19
	s_add_u32 s0, s3, s0
	s_addc_u32 s1, s2, s1
	global_load_dwordx4 v[18:21], v30, s[0:1] offset:48
	global_load_dwordx4 v[22:25], v30, s[0:1] offset:32
	global_load_dwordx4 v[26:29], v30, s[0:1] offset:16
	s_nop 0
	global_load_dwordx4 v[30:33], v30, s[0:1]
	s_movk_i32 s0, 0x3c00
	v_cmp_gt_i32_e32 vcc, s0, v34
	s_barrier
	s_and_saveexec_b64 s[2:3], vcc
	s_cbranch_execz .LBB0_882
	s_add_u32 s0, s6, s77
	s_addc_u32 s1, s7, 0
	s_add_u32 s0, s0, 0x12000
	s_addc_u32 s1, s1, 0
	v_lshrrev_b32_e32 v124, 8, v34
	v_and_b32_e32 v125, 0xff, v34
	v_lshlrev_b32_e32 v126, 4, v125
	v_and_b32_e32 v127, 3, v125
	v_lshlrev_b32_e32 v127, 10, v127
	v_lshrrev_b32_e32 v128, 2, v125
	v_lshlrev_b32_e32 v128, 4, v128
	v_add_u32_e32 v127, v127, v128
	v_add_u32_e32 v127, 0x8000, v127
	v_add_u32_e32 v129, 0, v124
	v_mul_u32_u24_e32 v130, 11, v129
	v_lshrrev_b32_e32 v130, 5, v130
	v_mul_u32_u24_e32 v164, 0x3000, v130
	v_lshl_add_u32 v164, v129, 12, v164
	v_add_u32_e32 v164, v164, v126
	global_load_dwordx4 v[132:135], v164, s[0:1]
	v_lshl_add_u32 v172, v129, 12, v127
	v_add_u32_e32 v129, 2, v124
	v_mul_u32_u24_e32 v130, 11, v129
	v_lshrrev_b32_e32 v130, 5, v130
	v_mul_u32_u24_e32 v165, 0x3000, v130
	v_lshl_add_u32 v165, v129, 12, v165
	v_add_u32_e32 v165, v165, v126
	global_load_dwordx4 v[136:139], v165, s[0:1]
	v_lshl_add_u32 v173, v129, 12, v127
	v_add_u32_e32 v129, 4, v124
	v_mul_u32_u24_e32 v130, 11, v129
	v_lshrrev_b32_e32 v130, 5, v130
	v_mul_u32_u24_e32 v166, 0x3000, v130
	v_lshl_add_u32 v166, v129, 12, v166
	v_add_u32_e32 v166, v166, v126
	global_load_dwordx4 v[140:143], v166, s[0:1]
	v_lshl_add_u32 v174, v129, 12, v127
	v_add_u32_e32 v129, 6, v124
	v_mul_u32_u24_e32 v130, 11, v129
	v_lshrrev_b32_e32 v130, 5, v130
	v_mul_u32_u24_e32 v167, 0x3000, v130
	v_lshl_add_u32 v167, v129, 12, v167
	v_add_u32_e32 v167, v167, v126
	global_load_dwordx4 v[144:147], v167, s[0:1]
	v_lshl_add_u32 v175, v129, 12, v127
	v_add_u32_e32 v129, 8, v124
	v_mul_u32_u24_e32 v130, 11, v129
	v_lshrrev_b32_e32 v130, 5, v130
	v_mul_u32_u24_e32 v168, 0x3000, v130
	v_lshl_add_u32 v168, v129, 12, v168
	v_add_u32_e32 v168, v168, v126
	global_load_dwordx4 v[148:151], v168, s[0:1]
	v_lshl_add_u32 v176, v129, 12, v127
	v_add_u32_e32 v129, 10, v124
	v_mul_u32_u24_e32 v130, 11, v129
	v_lshrrev_b32_e32 v130, 5, v130
	v_mul_u32_u24_e32 v169, 0x3000, v130
	v_lshl_add_u32 v169, v129, 12, v169
	v_add_u32_e32 v169, v169, v126
	global_load_dwordx4 v[152:155], v169, s[0:1]
	v_lshl_add_u32 v177, v129, 12, v127
	v_add_u32_e32 v129, 12, v124
	v_mul_u32_u24_e32 v130, 11, v129
	v_lshrrev_b32_e32 v130, 5, v130
	v_mul_u32_u24_e32 v170, 0x3000, v130
	v_lshl_add_u32 v170, v129, 12, v170
	v_add_u32_e32 v170, v170, v126
	global_load_dwordx4 v[156:159], v170, s[0:1]
	v_lshl_add_u32 v178, v129, 12, v127
	v_add_u32_e32 v129, 14, v124
	v_mul_u32_u24_e32 v130, 11, v129
	v_lshrrev_b32_e32 v130, 5, v130
	v_mul_u32_u24_e32 v171, 0x3000, v130
	v_lshl_add_u32 v171, v129, 12, v171
	v_add_u32_e32 v171, v171, v126
	global_load_dwordx4 v[160:163], v171, s[0:1]
	v_lshl_add_u32 v179, v129, 12, v127
	s_waitcnt vmcnt(7)
	ds_write_b128 v172, v[132:135]
	s_waitcnt vmcnt(6)
	ds_write_b128 v173, v[136:139]
	s_waitcnt vmcnt(5)
	ds_write_b128 v174, v[140:143]
	s_waitcnt vmcnt(4)
	ds_write_b128 v175, v[144:147]
	s_waitcnt vmcnt(3)
	ds_write_b128 v176, v[148:151]
	s_waitcnt vmcnt(2)
	ds_write_b128 v177, v[152:155]
	s_waitcnt vmcnt(1)
	ds_write_b128 v178, v[156:159]
	s_waitcnt vmcnt(0)
	ds_write_b128 v179, v[160:163]

.LBB0_944:
	s_or_b64 exec, exec, s[4:5]
.LBB0_945:
	s_or_b64 exec, exec, s[2:3]
	s_lshl_b64 s[0:1], s[24:25], 10
	s_waitcnt vmcnt(4)
	v_mov_b32_e32 v14, v0
	v_writelane_b32 v247, s0, 36
	s_waitcnt lgkmcnt(0)
	s_barrier
	s_cmp_ge_i32 s95, s96
	s_movk_i32 s2, 0x400
	v_readfirstlane_b32 s26, v14
	v_writelane_b32 v247, s1, 37
	s_cbranch_scc1 .Lp8_conv
	v_lshlrev_b32_e32 v4, 4, v14
	v_add_u32_e32 v2, 0x2000, v4
	v_ashrrev_i32_e32 v3, 31, v2
	v_lshrrev_b32_e32 v3, 22, v3
	v_add_u32_e32 v3, v2, v3
	v_ashrrev_i32_e32 v3, 10, v3
	v_mul_i32_i24_e32 v5, 0x400, v3
	v_sub_u32_e32 v2, v2, v5
	v_lshrrev_b32_e32 v5, 4, v2
	v_bitop3_b32 v5, v5, v2, 32 bitop3:0x6c
	v_ashrrev_i32_e32 v2, 31, v5
	v_lshrrev_b32_e32 v2, 26, v2
	v_add_u32_e32 v6, v5, v2
	v_lshlrev_b32_e32 v7, 3, v3
	v_ashrrev_i32_e32 v2, 6, v6
	v_and_b32_e32 v7, 0x7ffffff0, v7
	v_add_u32_e32 v7, v2, v7
	v_lshlrev_b32_e32 v2, 5, v3
	v_and_b32_e32 v2, 32, v2
	v_mad_u64_u32 v[2:3], s[8:9], v7, s2, v[2:3]
	v_and_b32_e32 v3, 0xc0, v6
	v_sub_u32_e32 v3, v5, v3
	s_lshl_b32 s0, s91, 11
	v_readlane_b32 s1, v247, 8
	v_ashrrev_i16_sdwa v3, v233, sext(v3) dst_sel:DWORD dst_unused:UNUSED_PAD src0_sel:DWORD src1_sel:BYTE_0
	s_add_u32 s27, s1, s0
	v_readlane_b32 s0, v247, 9
	v_bfe_i32 v3, v3, 0, 16
	s_addc_u32 s28, s0, 0
	v_add_lshl_u32 v134, v2, v3, 1
	v_bfe_i32 v2, v14, 27, 1
	s_and_b64 s[0:1], s[70:71], exec
	v_lshrrev_b32_e32 v2, 22, v2
	s_mov_b32 s0, 0x8cc000
	v_add_u32_e32 v2, v4, v2
	s_cselect_b32 s0, s0, 0x924c000
	v_and_b32_e32 v2, 0xfffffc00, v2
	s_add_u32 s29, s42, s0
	v_sub_u32_e32 v2, v4, v2
	s_addc_u32 s30, s43, 0
	s_and_b32 s31, s96, 4
	v_lshrrev_b32_e32 v3, 4, v2
	v_readlane_b32 s5, v247, 14
	v_bitop3_b32 v4, v3, v2, 32 bitop3:0x6c
	v_ashrrev_i32_e32 v3, 31, v14
	s_sub_i32 s0, s5, s31
	s_mul_i32 s34, s31, 17
	s_ashr_i32 s1, s26, 6
	s_ashr_i32 s3, s2, 31
	v_lshrrev_b32_e32 v3, 26, v3
	s_lshl_b32 s0, s0, 4
	s_ashr_i32 s4, s26, 8
	s_lshl_b64 s[6:7], s[2:3], 8
	s_lshl_b32 s35, s1, 10
	v_ashrrev_i32_e32 v2, 31, v4
	v_add_u32_e32 v3, v14, v3
	s_add_i32 s0, s0, s34
	v_lshrrev_b32_e32 v2, 26, v2
	v_ashrrev_i32_e32 v3, 6, v3
	s_cmp_lt_i32 s5, s31
	s_mul_i32 s5, s5, 17
	v_add_u32_e32 v5, v4, v2
	v_lshlrev_b32_e32 v6, 3, v3
	s_cselect_b32 s0, s5, s0
	v_readlane_b32 s5, v247, 13
	v_ashrrev_i32_e32 v2, 6, v5
	v_and_b32_e32 v6, 0x7ffffff0, v6
	s_add_i32 s0, s0, s5
	v_add_u32_e32 v6, v2, v6
	v_lshlrev_b32_e32 v2, 5, v3
	s_ashr_i32 s5, s0, 31
	v_and_b32_e32 v2, 32, v2
	s_lshr_b32 s5, s5, 29
	v_mad_u64_u32 v[2:3], s[8:9], v6, s2, v[2:3]
	s_add_i32 s5, s0, s5
	v_and_b32_e32 v3, 0xc0, v5
	s_and_b32 s5, s5, -8
	v_sub_u32_e32 v3, v4, v3
	s_sub_i32 s8, s96, s5
	v_ashrrev_i16_sdwa v3, v233, sext(v3) dst_sel:DWORD dst_unused:UNUSED_PAD src0_sel:DWORD src1_sel:BYTE_0
	s_min_i32 s10, s8, 8
	v_bfe_i32 v3, v3, 0, 16
	s_sub_i32 s11, s0, s5
	s_sext_i32_i8 s0, s10
	v_add_lshl_u32 v68, v2, v3, 1
	v_cvt_f32_i32_e32 v3, s0
	v_cvt_f32_i32_e32 v2, s11
	s_xor_b32 s8, s11, s0
	s_ashr_i32 s8, s8, 30
	v_rcp_iflag_f32_e32 v4, v3
	s_or_b32 s12, s8, 1
	s_mov_b32 s66, s24
	v_mov_b32_e32 v135, v69
	v_mul_f32_e32 v4, v2, v4
	v_trunc_f32_e32 v4, v4
	v_fma_f32 v2, -v4, v3, v2
	v_cvt_i32_f32_e32 v4, v4
	v_cmp_ge_f32_e64 s[8:9], |v2|, |v3|
	s_and_b64 s[8:9], s[8:9], exec
	s_cselect_b32 s0, s12, 0
	v_readfirstlane_b32 s8, v4
	s_add_i32 s0, s8, s0
	s_mul_i32 s8, s0, s10
	s_sub_i32 s8, s11, s8
	s_sext_i32_i8 s8, s8
	s_add_i32 s10, s5, s8
	s_ashr_i32 s11, s10, 31
	s_bfe_i64 s[12:13], s[0:1], 0x80000
	s_lshl_b64 s[8:9], s[10:11], 19
	s_lshl_b64 s[12:13], s[12:13], 19
	s_add_u32 s22, s29, s12
	s_addc_u32 s23, s30, s13
	s_add_i32 s11, s35, 0
	s_add_i32 m0, s11, 0x10000
	v_lshl_add_u64 v[2:3], s[22:23], 0, v[68:69]
	global_load_lds_dwordx4 v68, s[22:23]
	s_add_i32 m0, s11, 0x12000
	s_add_u32 s24, s27, s8
	global_load_lds_dwordx4 v134, s[22:23]
	s_addc_u32 s25, s28, s9
	s_mov_b32 m0, s11
	s_add_i32 s37, s11, 0x2000
	global_load_lds_dwordx4 v68, s[24:25]
	s_mov_b32 m0, s37
	s_add_u32 s8, s22, s6
	global_load_lds_dwordx4 v134, s[24:25]
	s_addc_u32 s9, s23, s7
	s_add_i32 m0, s11, 0x14000
	v_lshl_add_u64 v[10:11], s[8:9], 0, v[68:69]
	global_load_lds_dwordx4 v68, s[8:9]
	s_add_i32 m0, s11, 0x16000
	v_lshl_add_u64 v[12:13], s[8:9], 0, v[134:135]
	global_load_lds_dwordx4 v134, s[8:9]
	s_add_u32 s8, s24, s6
	s_addc_u32 s9, s25, s7
	s_add_i32 s38, s11, 0x4000
	s_mov_b32 m0, s38
	s_add_i32 s39, s11, 0x6000
	global_load_lds_dwordx4 v68, s[8:9]
	s_mov_b32 m0, s39
	v_lshl_add_u64 v[4:5], s[22:23], 0, v[134:135]
	global_load_lds_dwordx4 v134, s[8:9]
	v_lshl_add_u64 v[6:7], s[24:25], 0, v[68:69]
	v_lshl_add_u64 v[8:9], s[24:25], 0, v[134:135]
	s_cmp_lg_u32 s4, 1
	s_cbranch_scc1 .LBB0_948
	s_barrier

.LBB0_1013:
	s_or_b64 exec, exec, s[4:5]
.LBB0_1014:
	s_or_b64 exec, exec, s[2:3]
	v_mov_b32_e32 v18, v0
	s_movk_i32 s0, 0x100
	s_waitcnt lgkmcnt(0)
	s_barrier
	s_mov_b64 s[86:87], s[42:43]
	s_mov_b32 s48, s95
	s_mov_b32 s4, s85
	v_readfirstlane_b32 s5, v18
	v_cmp_gt_i32_e64 s[2:3], s0, v18
	v_lshl_add_u32 v19, v18, 2, 0
	s_barrier
	s_and_saveexec_b64 s[0:1], s[2:3]
	ds_write_b32 v19, v69
	s_or_b64 exec, exec, s[0:1]
	v_mov_b32_e32 v2, 0x23f68
	s_waitcnt lgkmcnt(0)
	s_barrier
	s_lshl_b32 s66, s24, 8
	v_add_u32_e32 v2, 0, v2
	ds_read_b64 v[2:3], v2
	s_and_b64 s[0:1], s[70:71], exec
	s_movk_i32 s0, 0x7fff
	s_cselect_b32 s97, 0x83ff, s0
	s_ashr_i32 s49, s5, 6
	s_add_u32 s38, s86, 0x337cc000
	s_addc_u32 s39, s87, 0
	s_waitcnt lgkmcnt(0)
	v_readfirstlane_b32 s6, v2
	s_lshl_b64 s[0:1], s[66:67], 2
	v_and_b32_e32 v20, 63, v18
	v_readfirstlane_b32 s5, v3
	s_add_u32 s0, s6, s0
	s_addc_u32 s1, s5, s1
	v_lshlrev_b32_e32 v6, 4, v20
	global_load_dwordx4 v[2:5], v6, s[0:1]
	s_add_i32 s0, s4, s97
	s_xor_b32 s1, s0, s4
	s_abs_i32 s4, s4
	v_cvt_f32_u32_e32 v7, s4
	s_sub_i32 s5, 0, s4
	s_abs_i32 s0, s0
	s_ashr_i32 s1, s1, 31
	v_rcp_iflag_f32_e32 v7, v7
	v_lshlrev_b32_e32 v68, 2, v20
	v_mul_f32_e32 v7, 0x4f7ffffe, v7
	v_cvt_u32_f32_e32 v7, v7
	s_nop 0
	v_readfirstlane_b32 s6, v7
	s_mul_i32 s5, s5, s6
	s_mul_hi_u32 s5, s6, s5
	s_add_i32 s6, s6, s5
	s_mul_hi_u32 s5, s0, s6
	s_mul_i32 s6, s5, s4
	s_sub_i32 s0, s0, s6
	s_add_i32 s6, s5, 1
	s_sub_i32 s7, s0, s4
	s_cmp_ge_u32 s0, s4
	s_cselect_b32 s5, s6, s5
	s_cselect_b32 s0, s7, s0
	s_add_i32 s6, s5, 1
	s_cmp_ge_u32 s0, s4
	s_cselect_b32 s0, s6, s5
	s_xor_b32 s0, s0, s1
	s_sub_i32 s50, s0, s1
	s_mul_i32 s40, s50, s48
	s_add_i32 s51, s40, s91
	s_cmp_lt_i32 s49, s50
	s_cselect_b64 s[0:1], -1, 0
	s_cmp_ge_i32 s49, s50
	s_cbranch_scc1 .LBB0_1019
	s_add_i32 s4, s51, s49
	s_cmp_gt_i32 s4, 0x83ff
	s_cbranch_scc1 .LBB0_1019
	s_ashr_i32 s5, s4, 31
	s_lshl_b64 s[4:5], s[4:5], 10
	s_add_u32 s4, s38, s4
	s_addc_u32 s5, s39, s5
	v_lshlrev_b32_e32 v7, 2, v68
	global_load_dwordx4 v[10:13], v7, s[4:5]
	s_andn2_b64 vcc, exec, s[0:1]
	s_cbranch_vccz .LBB0_1020
	s_branch .LBB0_1106

.LBB0_1159:
	s_or_b64 exec, exec, s[4:5]
.LBB0_1160:
	s_or_b64 exec, exec, s[2:3]
	s_waitcnt lgkmcnt(0)
	v_mov_b32_e32 v2, v0
	s_barrier
	s_mov_b64 s[4:5], s[42:43]
	v_lshlrev_b32_e32 v3, 2, v2
	v_readfirstlane_b32 s0, v2
	v_and_b32_e32 v3, 0xfc, v3
	s_ashr_i32 s65, s0, 6
	v_lshlrev_b32_e32 v68, 2, v3
	s_mov_b32 s66, s95
	s_mov_b32 s69, s85
	s_lshl_b32 s2, s65, 5
	v_lshl_add_u64 v[4:5], s[4:5], 0, v[68:69]
	s_mov_b64 s[0:1], 0x35be4000
	v_lshl_add_u64 v[64:65], v[4:5], 0, s[0:1]
	v_mov_b32_e32 v4, 0
	s_cmp_lt_i32 s2, s69
	v_mov_b32_e32 v8, 0
	v_mov_b32_e32 v9, 0
	v_mov_b32_e32 v10, 0
	v_mov_b32_e32 v11, 0
	s_barrier
	s_cbranch_scc0 .LBB0_1162
	s_ashr_i32 s3, s2, 31
	s_lshl_b64 s[0:1], s[2:3], 10
	v_lshl_add_u64 v[6:7], v[64:65], 0, s[0:1]
	global_load_dwordx4 v[8:11], v[6:7], off

.LBB0_1297:
	s_or_b64 exec, exec, s[4:5]
.LBB0_1298:
	s_or_b64 exec, exec, s[2:3]
	v_mov_b32_e32 v8, v0
	s_mov_b64 s[0:1], s[42:43]
	s_mov_b32 s11, s95
	s_mov_b32 s10, s85
	s_waitcnt lgkmcnt(0)
	s_barrier
	global_load_dword v2, v237, s[0:1]
	v_cmp_gt_i32_e32 vcc, 24, v8
	s_barrier
	s_waitcnt vmcnt(0)
	v_readfirstlane_b32 s8, v2
	s_lshl_b32 s2, s8, 1
	s_and_saveexec_b64 s[4:5], vcc
	s_cbranch_execz .LBB0_1306
	s_ashr_i32 s3, s11, 31
	v_mov_b32_e32 v2, s11
	v_mov_b32_e32 v3, s3
	v_mad_i64_i32 v[6:7], s[6:7], s10, v8, v[2:3]
	s_ashr_i32 s3, s2, 31
	v_cmp_gt_i64_e32 vcc, s[2:3], v[6:7]
	v_mov_b32_e32 v5, 0
	v_mov_b32_e32 v4, 0
	v_mov_b32_e32 v3, 0
	v_mov_b32_e32 v2, 0
	s_and_saveexec_b64 s[6:7], vcc
	s_cbranch_execz .LBB0_1305
	v_ashrrev_i32_e32 v2, 31, v6
	s_ashr_i32 s9, s8, 31
	s_lshr_b32 s3, s3, 29
	v_lshrrev_b32_e32 v2, 29, v2
	s_lshr_b32 s9, s9, 30
	s_add_i32 s3, s2, s3
	v_add_u32_e32 v2, v6, v2
	s_add_i32 s8, s8, s9
	s_and_b32 s3, s3, -8
	v_and_b32_e32 v3, -8, v2
	s_ashr_i32 s12, s8, 2
	s_sub_i32 s13, s2, s3
	v_sub_u32_e32 v4, v6, v3
	v_cmp_le_i32_e32 vcc, s13, v4
	s_add_i32 s3, s12, 1
	s_and_saveexec_b64 s[8:9], vcc
	s_xor_b64 s[8:9], exec, s[8:9]
	v_subrev_u32_e32 v3, s13, v4
	s_mul_i32 s14, s13, s3
	v_mul_lo_u32 v3, v3, s12
	v_add_u32_e32 v3, s14, v3
	s_andn2_saveexec_b64 s[8:9], s[8:9]
	v_mul_lo_u32 v3, v4, s3
	s_or_b64 exec, exec, s[8:9]
	v_ashrrev_i32_e32 v2, 3, v2
	v_add_u32_e32 v6, v3, v2
	v_lshrrev_b32_e32 v2, 31, v6
	v_add_u32_e32 v7, v6, v2
	v_ashrrev_i32_e32 v2, 1, v7
	v_ashrrev_i32_e32 v3, 31, v2
	v_lshl_add_u64 v[2:3], v[2:3], 4, s[0:1]
	v_add_co_u32_e32 v2, vcc, 0x35d6c000, v2
	s_nop 1
	v_addc_co_u32_e32 v3, vcc, 0, v3, vcc
	global_load_dwordx4 v[2:5], v[2:3], off
	s_waitcnt vmcnt(0)
	v_and_b32_e32 v5, -2, v7
	v_sub_u32_e32 v5, v6, v5

.LBB0_1671:
	s_or_b64 exec, exec, s[4:5]
.LBB0_1672:
	s_or_b64 exec, exec, s[2:3]
	v_mov_b32_e32 v4, v0
	s_mov_b64 s[2:3], s[42:43]
	s_mov_b32 s4, s95
	s_mov_b32 s5, s85
	s_waitcnt lgkmcnt(0)
	v_mov_b32_e32 v2, 0x23fa0
	s_barrier
	v_mov_b32_e32 v18, 0x23fa8
	v_add_u32_e32 v2, 0, v2
	ds_read_b64 v[2:3], v2
	v_readfirstlane_b32 s0, v4
	s_ashr_i32 s6, s0, 6
	v_readlane_b32 s0, v247, 36
	v_readlane_b32 s1, v247, 37
	s_waitcnt lgkmcnt(0)
	v_readfirstlane_b32 s8, v2
	s_lshl_b64 s[0:1], s[0:1], 2
	v_and_b32_e32 v34, 63, v4
	v_readfirstlane_b32 s7, v3
	s_add_u32 s8, s8, s0
	s_addc_u32 s9, s7, s1
	v_lshlrev_b32_e32 v67, 6, v34
	global_load_dwordx4 v[2:5], v67, s[8:9] offset:48
	global_load_dwordx4 v[6:9], v67, s[8:9] offset:32
	global_load_dwordx4 v[10:13], v67, s[8:9] offset:16
	global_load_dwordx4 v[14:17], v67, s[8:9]
	s_lshl_b32 s4, s4, 3
	v_add_u32_e32 v18, 0, v18
	ds_read_b64 v[18:19], v18
	s_add_i32 s4, s4, s23
	s_add_i32 s4, s4, s6
	s_cmp_gt_i32 s4, 0x83ff
	s_waitcnt lgkmcnt(0)
	v_readfirstlane_b32 s7, v19
	v_readfirstlane_b32 s8, v18
	s_cbranch_scc1 .LBB0_1684
	v_readlane_b32 s9, v247, 38
	s_add_u32 s24, s2, s9
	s_addc_u32 s25, s3, 0
	s_add_u32 s26, s2, 0x2e000
	s_addc_u32 s27, s3, 0
	s_add_u32 s28, s2, 0x35adc000
	s_addc_u32 s29, s3, 0
	s_add_u32 s30, s2, 0x359d4000
	s_addc_u32 s31, s3, 0
	s_lshl_b32 s34, s5, 3
	v_lshlrev_b32_e32 v142, 4, v34
	s_add_u32 s0, s8, s0
	s_addc_u32 s1, s7, s1
	v_lshlrev_b32_e32 v68, 2, v142
	global_load_dwordx4 v[18:21], v68, s[0:1]
	global_load_dwordx4 v[22:25], v68, s[0:1] offset:16
	global_load_dwordx4 v[26:29], v68, s[0:1] offset:32
	global_load_dwordx4 v[30:33], v68, s[0:1] offset:48
	v_mov_b32_e32 v143, v69
	v_lshl_add_u64 v[36:37], s[2:3], 0, v[142:143]
	s_mov_b64 s[0:1], 0x411f2100
	v_lshlrev_b32_e32 v38, 1, v142
	v_mov_b32_e32 v39, v69
	v_lshl_add_u64 v[144:145], v[36:37], 0, s[0:1]
	v_lshl_add_u64 v[38:39], s[2:3], 0, v[38:39]
	s_mov_b64 s[0:1], 0x1cccc000
	v_lshl_add_u64 v[146:147], v[38:39], 0, s[0:1]
	s_mov_b64 s[0:1], 0x14a8c000
	v_lshl_add_u64 v[148:149], v[36:37], 0, s[0:1]
	s_lshl_b32 s0, s6, 12
	s_lshl_b32 s6, s5, 4
	s_add_i32 s35, s0, 0
	s_mov_b64 s[0:1], 0x250cc000
	s_ashr_i32 s5, s4, 31
	s_ashr_i32 s7, s6, 31
	v_lshl_add_u64 v[150:151], v[36:37], 0, s[0:1]
	s_lshl_b64 s[0:1], s[4:5], 11
	s_lshl_b64 s[8:9], s[6:7], 11
	s_lshl_b64 s[10:11], s[4:5], 10
	s_add_u32 s10, s10, 0x14a8c000
	s_addc_u32 s11, s11, 0
	v_lshlrev_b32_e32 v246, 5, v34
	v_mov_b32_e32 v153, s1
	v_or_b32_e32 v152, s0, v142
	v_mov_b32_e32 v155, s11
	v_or_b32_e32 v154, s10, v142
	s_lshl_b64 s[10:11], s[6:7], 10
	s_lshl_b64 s[12:13], s[4:5], 5
	s_lshl_b64 s[14:15], s[6:7], 5
	v_lshl_or_b32 v156, v34, 5, s0
	v_mov_b32_e32 v157, s1
	s_branch .LBB0_1675
